# hyena ctx unit prologue: six boundary loads issued without intermediate waits; MLA rope table loads issued together
# speedup vs baseline: 1.0324x; 1.0059x over previous
.LBB0_733:
	s_ashr_i32 s39, s38, 31
	s_lshl_b64 s[0:1], s[38:39], 11
	s_add_u32 s10, s48, s0
	v_mov_b32_e32 v4, v0
	s_addc_u32 s11, s49, s1
	s_add_u32 s0, s52, s0
	v_ashrrev_i32_e32 v5, 31, v4
	v_lshlrev_b64 v[6:7], 2, v[4:5]
	s_addc_u32 s1, s53, s1
	v_lshl_add_u64 v[8:9], s[10:11], 0, v[6:7]
	v_lshl_add_u64 v[6:7], s[0:1], 0, v[6:7]
	global_load_dword v1, v[8:9], off
	global_load_dword v5, v[6:7], off
	v_lshrrev_b32_e32 v2, 2, v4
	v_add_u32_e32 v2, v2, v4
	s_lshl_b64 s[40:41], s[38:39], 2
	v_lshl_add_u32 v2, v2, 2, 0
	s_add_u32 s0, s46, s40
	s_addc_u32 s1, s47, s41
	v_readlane_b32 s56, v248, 43
	v_readlane_b32 s64, v248, 51
	v_readlane_b32 s65, v248, 52
	v_readlane_b32 s66, v248, 53
	v_readlane_b32 s67, v248, 54
	v_readlane_b32 s68, v248, 55
	v_readlane_b32 s69, v248, 56
	v_readlane_b32 s70, v248, 57
	v_readlane_b32 s71, v248, 58
	s_mov_b64 s[20:21], s[64:65]
	v_readlane_b32 s57, v248, 44
	v_readlane_b32 s58, v248, 45
	v_readlane_b32 s59, v248, 46
	v_readlane_b32 s60, v248, 47
	v_readlane_b32 s61, v248, 48
	v_readlane_b32 s62, v248, 49
	v_readlane_b32 s63, v248, 50
	v_readlane_b32 s56, v248, 0
	v_readlane_b32 s57, v248, 1
	v_readlane_b32 s58, v248, 2
	v_readlane_b32 s59, v248, 3
	v_readlane_b32 s60, v248, 4
	v_readlane_b32 s61, v248, 5
	v_readlane_b32 s62, v248, 6
	v_readlane_b32 s63, v248, 7
	s_mov_b64 s[56:57], s[60:61]
	s_mov_b64 s[58:59], s[62:63]
	v_and_b32_e32 v6, 0xffffff00, v4
	v_ashrrev_i32_e32 v7, 31, v6
	v_and_b32_e32 v12, 0xff, v4
	v_cmp_ne_u32_e32 vcc, 0, v12
	v_mov_b32_e32 v19, 0
	v_mov_b32_e32 v15, 0
	s_mov_b64 s[22:23], s[66:67]
	s_mov_b64 s[24:25], s[68:69]
	s_mov_b64 s[26:27], s[70:71]
	s_waitcnt vmcnt(0)
	ds_write2st64_b32 v2, v1, v5 offset1:10
	global_load_dword v1, v3, s[0:1]
	global_load_dword v10, v3, s[0:1] offset:2048
	s_add_i32 s0, s38, s12
	s_ashr_i32 s1, s0, 31
	s_lshl_b64 s[0:1], s[0:1], 2
	s_add_u32 s0, s20, s0
	s_addc_u32 s1, s21, s1
	global_load_dword v5, v3, s[0:1]
	s_add_i32 s0, s38, s54
	s_ashr_i32 s1, s0, 31
	s_lshl_b64 s[0:1], s[0:1], 2
	s_add_u32 s0, s20, s0
	s_addc_u32 s1, s21, s1
	global_load_dword v11, v3, s[0:1]
	s_add_i32 s0, s38, 0x80
	s_mul_hi_i32 s1, s0, 0x4400
	s_mulk_i32 s0, 0x4400
	s_add_u32 s0, s58, s0
	s_addc_u32 s1, s59, s1
	v_lshl_add_u64 v[8:9], v[6:7], 1, s[0:1]
	s_mov_b64 s[20:21], 0x41c94000
	v_lshl_add_u64 v[8:9], v[8:9], 0, s[20:21]
	v_lshlrev_b32_e32 v2, 1, v12
	s_and_saveexec_b64 s[0:1], vcc
	s_cbranch_execz .LBB0_735
	v_lshl_add_u64 v[14:15], v[8:9], 0, v[2:3]
	global_load_ushort v15, v[14:15], off offset:-2
.LBB0_735:
	s_or_b64 exec, exec, s[0:1]
	v_lshl_add_u64 v[8:9], v[8:9], 0, v[2:3]
	global_load_ushort v14, v[8:9], off
	s_movk_i32 s0, 0xff
	v_cmp_ne_u32_e64 s[0:1], s0, v12
	s_and_saveexec_b64 s[10:11], s[0:1]
	s_cbranch_execz .LBB0_737
	global_load_ushort v19, v[8:9], off offset:2

.LBB0_739:
	s_or_b64 exec, exec, s[10:11]
	v_lshl_add_u64 v[8:9], v[8:9], 0, v[2:3]
	global_load_ushort v25, v[8:9], off
	s_and_saveexec_b64 s[10:11], s[0:1]
	s_cbranch_execz .LBB0_741
	global_load_ushort v21, v[8:9], off offset:2
.LBB0_741:
	s_or_b64 exec, exec, s[10:11]
	v_mov_b32_e32 v8, 0x3000
	global_load_dword v18, v3, s[40:41] offset:2048
	global_load_dword v24, v218, s[40:41]
	global_load_dword v22, v8, s[40:41] offset:2048
	v_readlane_b32 s56, v248, 0
	v_readlane_b32 s57, v248, 1
	v_readlane_b32 s58, v248, 2
	v_readlane_b32 s59, v248, 3
	v_readlane_b32 s60, v248, 4
	v_readlane_b32 s61, v248, 5
	s_add_i32 s10, s38, 0x480
	v_readlane_b32 s62, v248, 6
	v_readlane_b32 s63, v248, 7
	s_mov_b64 s[56:57], s[60:61]
	s_mul_hi_i32 s11, s10, 0x4400
	s_mulk_i32 s10, 0x4400
	s_mov_b64 s[58:59], s[62:63]
	s_add_u32 s10, s58, s10
	s_addc_u32 s11, s59, s11
	v_lshl_add_u64 v[8:9], v[6:7], 1, s[10:11]
	v_lshl_add_u64 v[8:9], v[8:9], 0, s[20:21]
	v_mov_b32_e32 v7, 0
	v_mov_b32_e32 v23, 0
	s_and_saveexec_b64 s[10:11], vcc
	s_cbranch_execz .LBB0_743
	v_lshl_add_u64 v[26:27], v[8:9], 0, v[2:3]
	global_load_ushort v23, v[26:27], off offset:-2
.LBB0_743:
	s_or_b64 exec, exec, s[10:11]
	v_lshl_add_u64 v[8:9], v[8:9], 0, v[2:3]
	global_load_ushort v2, v[8:9], off
	s_and_saveexec_b64 s[10:11], s[0:1]
	s_cbranch_execz .LBB0_745
	global_load_ushort v7, v[8:9], off offset:2
.LBB0_745:
	s_or_b64 exec, exec, s[10:11]
	v_mov_b32_e32 v8, 0x4000
	global_load_dword v26, v218, s[40:41] offset:2048
	global_load_dword v27, v8, s[40:41]
	v_mov_b32_e32 v8, 0x1000
	global_load_dword v28, v8, s[40:41]
	s_waitcnt vmcnt(3)
	v_lshlrev_b32_e32 v15, 16, v15
	v_lshlrev_b32_e32 v19, 16, v19
	v_lshlrev_b32_e32 v17, 16, v17
	v_lshlrev_b32_e32 v21, 16, v21
	v_lshlrev_b32_e32 v23, 16, v23
	v_lshlrev_b32_e32 v7, 16, v7
	v_lshlrev_b32_e32 v29, 16, v2
	v_lshlrev_b32_e32 v2, 16, v25
	v_lshlrev_b32_e32 v9, 16, v14
	v_mul_f32_e32 v2, v24, v2
	s_mul_i32 s0, s38, 0x4400
	v_lshlrev_b32_e32 v14, 2, v4
	v_add3_u32 v8, v6, v12, s84
	v_mul_f32_e32 v6, v13, v9
	v_readlane_b32 s10, v251, 44
	v_fmac_f32_e32 v2, v17, v18
	s_mul_hi_i32 s1, s38, 0x4400
	v_ashrrev_i32_e32 v25, 7, v4
	v_lshlrev_b32_e32 v30, 4, v4
	v_and_b32_e32 v4, 63, v4
	v_readlane_b32 s11, v251, 45
	s_add_u32 s0, s10, s0
	v_and_b32_e32 v13, 0x100, v14
	v_fmac_f32_e32 v6, v15, v16
	v_fmac_f32_e32 v2, v21, v22
	v_add_u32_e32 v12, 0, v14
	v_lshlrev_b32_e32 v24, 6, v25
	v_lshl_add_u32 v31, v25, 11, 0
	v_and_b32_e32 v30, 0x3f0, v30
	v_ashrrev_i32_e32 v9, 31, v8
	v_lshlrev_b32_e32 v32, 2, v4
	v_lshlrev_b32_e32 v14, 8, v25
	v_lshlrev_b32_e32 v4, 4, v4
	s_addc_u32 s1, s11, s1
	v_lshlrev_b32_e32 v25, 2, v13
	v_fmac_f32_e32 v6, v19, v20
	v_or_b32_e32 v15, 48, v24
	v_add_u32_e32 v16, -16, v24
	v_sub_u32_e32 v17, 0, v32
	v_sub_u32_e32 v18, 0, v4
	v_add3_u32 v19, v31, v25, v30
	v_lshl_add_u64 v[8:9], v[8:9], 1, s[0:1]
	v_mul_f32_e32 v20, v5, v6
	s_mov_b64 s[40:41], -1
	ds_write2st64_b32 v12, v6, v2 offset0:20 offset1:28
	s_waitcnt vmcnt(2)
	v_mul_f32_e32 v21, v26, v29
	s_waitcnt vmcnt(0)
	v_fmac_f32_e32 v21, v23, v28
	v_fmac_f32_e32 v21, v7, v27
	ds_write_b32 v12, v21 offset:9216
	s_branch .LBB0_747

.LBB0_1223:
	s_andn2_b64 vcc, exec, s[0:1]
	s_mov_b32 s12, 4
	s_cbranch_vccnz .LBB0_1225
	v_or_b32_e32 v1, s4, v14
	v_lshlrev_b32_e32 v4, 4, v1
	v_ashrrev_i32_e32 v5, 31, v4
	v_mov_b32_e32 v1, v222
	v_mov_b32_e32 v2, v222
	v_lshl_add_u64 v[4:5], v[4:5], 3, s[70:71]
	global_load_dwordx4 v[186:189], v[4:5], off
	global_load_dwordx4 v[190:193], v[4:5], off offset:16
	global_load_dwordx4 v[194:197], v[4:5], off offset:32
	global_load_dwordx4 v[198:201], v[4:5], off offset:48
	global_load_dwordx4 v[202:205], v[4:5], off offset:64
	global_load_dwordx4 v[206:209], v[4:5], off offset:80
	global_load_dwordx4 v[226:229], v[4:5], off offset:96
	global_load_dwordx4 v[230:233], v[4:5], off offset:112
	v_lshlrev_b32_e32 v1, 2, v1
	v_lshlrev_b32_e32 v2, 2, v2
	v_xor_b32_e32 v1, 0x80, v1
	v_xor_b32_e32 v2, 0x80, v2
	s_waitcnt vmcnt(9)
	v_lshlrev_b32_e32 v10, 16, v130
	v_and_b32_e32 v11, 0xffff0000, v130
	ds_bpermute_b32 v1, v1, v10
	ds_bpermute_b32 v2, v2, v11
	v_cmp_eq_u32_e32 vcc, 0, v15
	s_movk_i32 s12, 0x44
	s_waitcnt vmcnt(7)
	v_mov_b32_e32 v13, v188
	s_waitcnt lgkmcnt(1)
	v_cndmask_b32_e64 v18, v1, -v1, vcc
	s_waitcnt lgkmcnt(0)
	v_cndmask_b32_e64 v19, v2, -v2, vcc
	v_mov_b32_e32 v8, v187
	v_mov_b32_e32 v9, v189
	v_mov_b32_e32 v12, v186
	v_pk_mul_f32 v[6:7], v[18:19], v[8:9]
	v_mov_b32_e32 v1, v222
	v_pk_fma_f32 v[6:7], v[12:13], v[10:11], v[6:7]
	v_mov_b32_e32 v2, v222
	v_cvt_pk_bf16_f32 v130, v6, v7
	v_lshlrev_b32_e32 v1, 2, v1
	v_lshlrev_b32_e32 v2, 2, v2
	v_xor_b32_e32 v1, 0x80, v1
	v_xor_b32_e32 v2, 0x80, v2
	v_lshlrev_b32_e32 v10, 16, v131
	v_and_b32_e32 v11, 0xffff0000, v131
	ds_bpermute_b32 v1, v1, v10
	ds_bpermute_b32 v2, v2, v11
	s_waitcnt lgkmcnt(1)
	v_cndmask_b32_e64 v18, v1, -v1, vcc
	s_waitcnt lgkmcnt(0)
	v_cndmask_b32_e64 v19, v2, -v2, vcc
	v_mov_b32_e32 v1, v222
	v_mov_b32_e32 v2, v222
	s_waitcnt vmcnt(6)
	v_mov_b32_e32 v13, v192
	v_mov_b32_e32 v8, v191
	v_mov_b32_e32 v9, v193
	v_mov_b32_e32 v12, v190
	v_pk_mul_f32 v[6:7], v[18:19], v[8:9]
	v_lshlrev_b32_e32 v1, 2, v1
	v_pk_fma_f32 v[6:7], v[12:13], v[10:11], v[6:7]
	v_lshlrev_b32_e32 v2, 2, v2
	v_cvt_pk_bf16_f32 v131, v6, v7
	v_xor_b32_e32 v1, 0x80, v1
	v_xor_b32_e32 v2, 0x80, v2
	v_lshlrev_b32_e32 v10, 16, v132
	v_and_b32_e32 v11, 0xffff0000, v132
	ds_bpermute_b32 v1, v1, v10
	ds_bpermute_b32 v2, v2, v11
	s_waitcnt lgkmcnt(1)
	v_cndmask_b32_e64 v18, v1, -v1, vcc
	s_waitcnt lgkmcnt(0)
	v_cndmask_b32_e64 v19, v2, -v2, vcc
	v_mov_b32_e32 v1, v222
	v_mov_b32_e32 v2, v222
	s_waitcnt vmcnt(5)
	v_mov_b32_e32 v13, v196
	v_mov_b32_e32 v8, v195
	v_mov_b32_e32 v9, v197
	v_mov_b32_e32 v12, v194
	v_pk_mul_f32 v[6:7], v[18:19], v[8:9]
	v_lshlrev_b32_e32 v1, 2, v1
	v_pk_fma_f32 v[6:7], v[12:13], v[10:11], v[6:7]
	v_lshlrev_b32_e32 v2, 2, v2
	v_cvt_pk_bf16_f32 v132, v6, v7
	v_xor_b32_e32 v1, 0x80, v1
	v_xor_b32_e32 v2, 0x80, v2
	v_lshlrev_b32_e32 v10, 16, v133
	v_and_b32_e32 v11, 0xffff0000, v133
	ds_bpermute_b32 v1, v1, v10
	ds_bpermute_b32 v2, v2, v11
	s_waitcnt lgkmcnt(1)
	v_cndmask_b32_e64 v18, v1, -v1, vcc
	s_waitcnt lgkmcnt(0)
	v_cndmask_b32_e64 v19, v2, -v2, vcc
	v_mov_b32_e32 v1, v222
	v_mov_b32_e32 v2, v222
	s_waitcnt vmcnt(4)
	v_mov_b32_e32 v13, v200
	v_mov_b32_e32 v8, v199
	v_mov_b32_e32 v9, v201
	v_mov_b32_e32 v12, v198
	v_pk_mul_f32 v[6:7], v[18:19], v[8:9]
	v_lshlrev_b32_e32 v1, 2, v1
	v_pk_fma_f32 v[6:7], v[12:13], v[10:11], v[6:7]
	v_lshlrev_b32_e32 v2, 2, v2
	v_cvt_pk_bf16_f32 v133, v6, v7
	v_xor_b32_e32 v1, 0x80, v1
	v_xor_b32_e32 v2, 0x80, v2
	v_lshlrev_b32_e32 v10, 16, v134
	v_and_b32_e32 v11, 0xffff0000, v134
	ds_bpermute_b32 v1, v1, v10
	ds_bpermute_b32 v2, v2, v11
	s_waitcnt lgkmcnt(1)
	v_cndmask_b32_e64 v18, v1, -v1, vcc
	s_waitcnt lgkmcnt(0)
	v_cndmask_b32_e64 v19, v2, -v2, vcc
	v_mov_b32_e32 v1, v222
	v_mov_b32_e32 v2, v222
	s_waitcnt vmcnt(3)
	v_mov_b32_e32 v13, v204
	v_mov_b32_e32 v8, v203
	v_mov_b32_e32 v9, v205
	v_mov_b32_e32 v12, v202
	v_pk_mul_f32 v[6:7], v[18:19], v[8:9]
	v_lshlrev_b32_e32 v1, 2, v1
	v_pk_fma_f32 v[6:7], v[12:13], v[10:11], v[6:7]
	v_lshlrev_b32_e32 v2, 2, v2
	v_cvt_pk_bf16_f32 v134, v6, v7
	v_xor_b32_e32 v1, 0x80, v1
	v_xor_b32_e32 v2, 0x80, v2
	v_lshlrev_b32_e32 v10, 16, v135
	v_and_b32_e32 v11, 0xffff0000, v135
	ds_bpermute_b32 v1, v1, v10
	ds_bpermute_b32 v2, v2, v11
	s_waitcnt lgkmcnt(1)
	v_cndmask_b32_e64 v18, v1, -v1, vcc
	s_waitcnt lgkmcnt(0)
	v_cndmask_b32_e64 v19, v2, -v2, vcc
	v_mov_b32_e32 v1, v222
	v_mov_b32_e32 v2, v222
	s_waitcnt vmcnt(2)
	v_mov_b32_e32 v13, v208
	v_mov_b32_e32 v8, v207
	v_mov_b32_e32 v9, v209
	v_mov_b32_e32 v12, v206
	v_pk_mul_f32 v[6:7], v[18:19], v[8:9]
	v_lshlrev_b32_e32 v1, 2, v1
	v_pk_fma_f32 v[6:7], v[12:13], v[10:11], v[6:7]
	v_lshlrev_b32_e32 v2, 2, v2
	v_cvt_pk_bf16_f32 v135, v6, v7
	v_xor_b32_e32 v1, 0x80, v1
	v_xor_b32_e32 v2, 0x80, v2
	v_lshlrev_b32_e32 v10, 16, v136
	v_and_b32_e32 v11, 0xffff0000, v136
	ds_bpermute_b32 v1, v1, v10
	ds_bpermute_b32 v2, v2, v11
	s_waitcnt lgkmcnt(1)
	v_cndmask_b32_e64 v18, v1, -v1, vcc
	s_waitcnt lgkmcnt(0)
	v_cndmask_b32_e64 v19, v2, -v2, vcc
	v_mov_b32_e32 v1, v222
	v_mov_b32_e32 v2, v222
	s_waitcnt vmcnt(1)
	v_mov_b32_e32 v13, v228
	v_mov_b32_e32 v8, v227
	v_mov_b32_e32 v9, v229
	v_mov_b32_e32 v12, v226
	v_pk_mul_f32 v[6:7], v[18:19], v[8:9]
	v_lshlrev_b32_e32 v1, 2, v1
	v_pk_fma_f32 v[6:7], v[12:13], v[10:11], v[6:7]
	v_lshlrev_b32_e32 v2, 2, v2
	v_cvt_pk_bf16_f32 v136, v6, v7
	v_xor_b32_e32 v1, 0x80, v1
	v_xor_b32_e32 v2, 0x80, v2
	v_lshlrev_b32_e32 v8, 16, v137
	v_and_b32_e32 v9, 0xffff0000, v137
	ds_bpermute_b32 v1, v1, v8
	ds_bpermute_b32 v2, v2, v9
	s_waitcnt lgkmcnt(1)
	v_cndmask_b32_e64 v12, v1, -v1, vcc
	s_waitcnt lgkmcnt(0)
	v_cndmask_b32_e64 v13, v2, -v2, vcc
	s_waitcnt vmcnt(0)
	v_mov_b32_e32 v11, v232
	v_mov_b32_e32 v6, v231
	v_mov_b32_e32 v7, v233
	v_mov_b32_e32 v10, v230
	v_pk_mul_f32 v[4:5], v[12:13], v[6:7]
	s_nop 0
	v_pk_fma_f32 v[4:5], v[10:11], v[8:9], v[4:5]
	s_nop 0
	v_cvt_pk_bf16_f32 v137, v4, v5
